# expert GEMM prologue: tiles 0 and 1 of the first unit requested together (second into free accumulator registers)
# baseline (speedup 1.0000x reference)
;     __device__ __forceinline__ int blane(int rho) const { if constexpr (NPN == 2) return rho; else return 64 * (rho >> 5) + 16 * ((rho >> 3) & 3) + (rho & 7); }
; template <class Epi, class Sched, bool ALIGN_EPI>
; __device__ __forceinline__ void gemm_phase(LAS unsigned char* lds, const Gemm g, const Sched& S, const Epi& E) {
;     ...
;     [[maybe_unused]] const int bh = wid >> 2, brg = ((wid & 3) << 3) + (lane & 7), bkg = lane >> 3;
;     [[maybe_unused]] const int brho = 32 * (brg >> 3) + 8 * (brg & 3) + 4 * ((brg >> 2) & 1);
;     [[maybe_unused]] const int bwofs = bh * HTB + lds_byte(4 * brg, 8 * bkg);
;     [[maybe_unused]] const unsigned blane = (unsigned)(S.blane(brho) + 8 * bkg * Sched::LDN) * 4u;
;     [[maybe_unused]] const unsigned bwaddr = ((unsigned)(size_t)lds + (unsigned)bwofs) | ((unsigned)(brg & 3) << 6);
.LBB0_2233:
	s_ashr_i32 s3, s2, 6
	s_lshl_b32 s1, s3, 10
	s_lshl_b32 s3, s3, 5
	v_and_b32_e32 v3, 3, v1
	s_and_b32 s30, s3, 0x60
	v_lshlrev_b32_e32 v4, 3, v3
	v_and_b32_e32 v5, 4, v1
	v_lshlrev_b32_e32 v34, 2, v1
	v_or3_b32 v4, v4, v5, s30
	v_and_or_b32 v5, v34, 16, s3
	v_lshrrev_b32_e32 v5, 3, v5
	v_bfe_u32 v6, v1, 5, 1
	s_ashr_i32 s0, s2, 8
	v_and_or_b32 v5, v5, 14, v6
	v_lshlrev_b32_e32 v6, 8, v1
	v_lshlrev_b32_e32 v7, 1, v1
	v_lshlrev_b32_e32 v35, 4, v1
	v_and_b32_e32 v2, 56, v1
	s_lshl_b32 s6, s0, 14
	v_and_b32_e32 v6, 0x300, v6
	v_and_b32_e32 v7, 48, v7
	v_and_b32_e32 v8, 32, v35
	v_lshlrev_b32_e32 v5, 10, v5
	v_bitop3_b32 v6, v6, v8, v7 bitop3:0x36
	v_lshlrev_b32_e32 v2, 10, v2
	s_add_i32 s6, s6, 0
	v_lshl_or_b32 v231, v4, 2, v2
	v_add3_u32 v2, s6, v6, v5
	v_lshl_or_b32 v232, v3, 6, v2
	v_mov_b32_e32 v2, v1
	v_mov_b32_e32 v233, 1
	v_ashrrev_i32_e32 v4, 31, v2
	v_lshrrev_b32_e32 v4, 26, v4
	v_lshlrev_b32_e32 v3, 4, v2
	v_add_u32_e32 v4, v2, v4
	v_bfe_i32 v2, v2, 27, 1
	v_lshrrev_b32_e32 v2, 22, v2
	v_add_u32_e32 v2, v3, v2
	v_and_b32_e32 v2, 0xfffffc00, v2
	v_sub_u32_e32 v2, v3, v2
	v_lshrrev_b32_e32 v5, 4, v2
	v_bitop3_b32 v2, v5, v2, 32 bitop3:0x6c
	v_ashrrev_i32_e32 v6, 31, v2
	v_lshrrev_b32_e32 v6, 26, v6
	v_add_u32_e32 v6, v2, v6
	v_ashrrev_i32_e32 v7, 6, v6
	v_and_b32_e32 v6, 0xc0, v6
	v_ashrrev_i32_e32 v4, 6, v4
	v_sub_u32_e32 v2, v2, v6
	v_lshlrev_b32_e32 v5, 3, v4
	v_lshlrev_b32_e32 v4, 5, v4
	v_ashrrev_i16_sdwa v2, v233, sext(v2) dst_sel:DWORD dst_unused:UNUSED_PAD src0_sel:DWORD src1_sel:BYTE_0
	v_and_b32_e32 v4, 32, v4
	v_bfe_i32 v2, v2, 0, 16
	v_add_lshl_u32 v36, v4, v2, 1
	v_add_u32_e32 v2, 0x2000, v3
	v_ashrrev_i32_e32 v3, 31, v2
	v_lshrrev_b32_e32 v3, 22, v3
	v_add_u32_e32 v3, v2, v3
	v_ashrrev_i32_e32 v3, 10, v3
	v_mul_i32_i24_e32 v4, 0x400, v3
	v_sub_u32_e32 v2, v2, v4
	v_lshrrev_b32_e32 v4, 4, v2
	v_bitop3_b32 v2, v4, v2, 32 bitop3:0x6c
	v_ashrrev_i32_e32 v6, 31, v2
	v_lshrrev_b32_e32 v6, 26, v6
	v_and_b32_e32 v5, -16, v5
	v_add_u32_e32 v6, v2, v6
	v_add_u32_e32 v5, v7, v5
	v_ashrrev_i32_e32 v7, 6, v6
	v_and_b32_e32 v6, 0xc0, v6
	v_sub_u32_e32 v2, v2, v6
	v_lshlrev_b32_e32 v4, 3, v3
	v_lshlrev_b32_e32 v3, 5, v3
	v_ashrrev_i16_sdwa v2, v233, sext(v2) dst_sel:DWORD dst_unused:UNUSED_PAD src0_sel:DWORD src1_sel:BYTE_0
	v_and_b32_e32 v3, 32, v3
	v_bfe_i32 v2, v2, 0, 16
	v_add_lshl_u32 v37, v3, v2, 1
	v_add_u32_e32 v2, s48, v5
	s_add_i32 s6, s33, -1
	v_min_i32_e32 v2, s6, v2
	v_readlane_b32 s8, v254, 47
	v_ashrrev_i32_e32 v3, 31, v2
	v_readlane_b32 s9, v254, 48
	v_and_b32_e32 v4, -16, v4
	v_add_u32_e32 v4, v7, v4
	v_lshl_add_u64 v[2:3], v[2:3], 2, s[8:9]
	global_load_dword v2, v[2:3], off
	s_add_i32 s7, s48, 0x80
	v_readlane_b32 s12, v253, 21
	s_cmpk_lt_u32 s2, 0x100
	v_readlane_b32 s20, v253, 29
	v_readlane_b32 s21, v253, 30
	v_readlane_b32 s22, v253, 31
	v_readlane_b32 s23, v253, 32
	v_readlane_b32 s24, v253, 33
	v_readlane_b32 s25, v253, 34
	v_readlane_b32 s26, v253, 35
	v_readlane_b32 s27, v253, 36
	s_mov_b64 s[20:21], s[24:25]
	s_mov_b64 s[22:23], s[26:27]
	s_mov_b32 s3, 0
	v_readlane_b32 s13, v253, 22
	v_readlane_b32 s14, v253, 23
	v_readlane_b32 s15, v253, 24
	v_readlane_b32 s16, v253, 25
	v_readlane_b32 s17, v253, 26
	v_readlane_b32 s18, v253, 27
	v_readlane_b32 s19, v253, 28
	s_waitcnt vmcnt(0)
	v_lshlrev_b32_e32 v38, 8, v2
	v_add_u32_e32 v2, s48, v4
	v_min_i32_e32 v2, s6, v2
	v_ashrrev_i32_e32 v3, 31, v2
	v_lshl_add_u64 v[2:3], v[2:3], 2, s[8:9]
	global_load_dword v2, v[2:3], off
	v_and_b32_e32 v38, 0xfffff800, v38
	v_add_u32_e32 v226, v36, v38
	s_waitcnt vmcnt(0)
	v_lshlrev_b32_e32 v39, 8, v2
	v_add_u32_e32 v2, s7, v5
	v_min_i32_e32 v2, s6, v2
	v_ashrrev_i32_e32 v3, 31, v2
	v_lshl_add_u64 v[2:3], v[2:3], 2, s[8:9]
	global_load_dword v2, v[2:3], off
	v_and_b32_e32 v38, 0xfffff800, v39
	v_add_u32_e32 v228, v37, v38
	s_waitcnt vmcnt(0)
	v_lshlrev_b32_e32 v2, 8, v2
	v_and_b32_e32 v40, 0xfffff800, v2
	v_add_u32_e32 v2, s7, v4
	v_min_i32_e32 v2, s6, v2
	v_ashrrev_i32_e32 v3, 31, v2
	v_lshl_add_u64 v[2:3], v[2:3], 2, s[8:9]
	global_load_dword v2, v[2:3], off
	s_cselect_b64 s[8:9], -1, 0
	s_and_b64 s[6:7], s[8:9], exec
	s_cselect_b32 s39, s20, s22
	s_cselect_b32 s38, s21, s23
	s_add_u32 s2, s39, s4
	s_addc_u32 s6, s38, s5
	s_lshl_b32 s4, s31, 7
	s_ashr_i32 s5, s4, 31
	s_lshl_b64 s[4:5], s[4:5], 2
	s_add_u32 s20, s2, s4
	s_addc_u32 s21, s6, s5
	s_add_u32 s4, s20, 0x1000
	s_addc_u32 s5, s21, 0
	s_add_i32 s40, s1, 0
	s_mov_b32 m0, s40
	s_add_i32 s41, s40, 0x2000
	s_add_i32 s42, s40, 0x4000
	v_add_u32_e32 v234, v36, v40
	s_add_i32 s43, s40, 0x6000
	v_mov_b32_e32 v36, v232
	s_waitcnt vmcnt(0)
; #define PG8_BWAIT(n) asm volatile("s_waitcnt vmcnt(" #n ")" : "+v"(bv[0]), "+v"(bv[1]), "+v"(bv[2]), "+v"(bv[3]), "+v"(bv[4]), "+v"(bv[5]), "+v"(bv[6]), "+v"(bv[7]) :: "memory")
; #define PG8_STAGE_A(bufoff, V0, V1, kb) do { \
;         __builtin_amdgcn_global_load_lds((const unsigned*)((Abase + (kb)) + (V0)), (LAS unsigned*)(lds + (bufoff) + ldsw), 16, 0, 0); \
;         __builtin_amdgcn_global_load_lds((const unsigned*)((Abase + (kb)) + (V1)), (LAS unsigned*)(lds + (bufoff) + ldsw + 8192), 16, 0, 0); } while (0)
; #define PG8_WAIT_V(n) asm volatile("s_waitcnt vmcnt(" #n ")" ::: "memory")
; #define PG8_WAIT_L(n) asm volatile("s_waitcnt lgkmcnt(" #n ")" ::: "memory")
; #define PG8_BAR __builtin_amdgcn_s_barrier()
; #define PG8_SCHED __builtin_amdgcn_sched_barrier(0)
; template <class Epi, class Sched, bool ALIGN_EPI>
; __device__ __forceinline__ void gemm_phase(LAS unsigned char* lds, const Gemm g, const Sched& S, const Epi& E) {
;     ...
;         PG8_BISSUE(pbc);
;         PG8_STAGE_A(PG8_SA(0, 0), vc00, vc01, 0u); PG8_STAGE_A(PG8_SA(0, 1), vc10, vc11, 0u); PG8_STAGE_A(PG8_SA(1, 0), vc00, vc01, 128u);
;         PG8_BWAIT(0); PG8_BCOMMIT(0); PG8_SCHED; PG8_BISSUE(pbc + (size_t)64 * Sched::LDN);
;         PG8_BWAIT(0); PG8_BCOMMIT(1); PG8_SCHED; PG8_BISSUE(pbc + (size_t)128 * Sched::LDN);
;         PG8_WAIT_V(8); PG8_WAIT_L(0);
;         if (wr == 1) PG8_BAR;
;         PG8_BAR; PG8_BAR;
	v_lshlrev_b32_e32 v2, 8, v2
	v_and_b32_e32 v41, 0xfffff800, v2
	global_load_dwordx4 v[2:5], v231, s[20:21] offset:0
	global_load_dwordx4 v[6:9], v231, s[20:21] offset:0x400
	global_load_dwordx4 v[10:13], v231, s[20:21] offset:0x800
	global_load_dwordx4 v[14:17], v231, s[20:21] offset:0xc00
	global_load_dwordx4 v[18:21], v231, s[4:5] offset:0
	global_load_dwordx4 v[22:25], v231, s[4:5] offset:0x400
	global_load_dwordx4 v[26:29], v231, s[4:5] offset:0x800
	global_load_dwordx4 v[30:33], v231, s[4:5] offset:0xc00
	v_readlane_b32 s4, v255, 13
	v_readlane_b32 s5, v255, 14
	v_add_u32_e32 v235, v37, v41
	s_nop 3
	global_load_lds_dwordx4 v226, s[4:5]
	s_mov_b32 m0, s41
	s_nop 0
	global_load_lds_dwordx4 v228, s[4:5]
	s_mov_b32 m0, s42
	s_nop 0
	global_load_lds_dwordx4 v234, s[4:5]
	s_mov_b32 m0, s43
	s_nop 0
	global_load_lds_dwordx4 v235, s[4:5]
	s_add_u32 s4, s90, 0x176c0080
	s_addc_u32 s5, s91, 0
	s_add_i32 s44, s40, 0x8000
	s_mov_b32 m0, s44
	s_add_i32 s45, s40, 0xa000
	global_load_lds_dwordx4 v226, s[4:5]
	s_mov_b32 m0, s45
	s_nop 0
	global_load_lds_dwordx4 v228, s[4:5]
	s_add_u32 s4, s20, 0x10000
	s_addc_u32 s5, s21, 0
	global_load_dwordx4 v[42:45], v231, s[4:5] offset:0
	global_load_dwordx4 v[46:49], v231, s[4:5] offset:0x400
	global_load_dwordx4 v[50:53], v231, s[4:5] offset:0x800
	global_load_dwordx4 v[54:57], v231, s[4:5] offset:0xc00
	s_add_u32 s4, s4, 0x1000
	s_addc_u32 s5, s5, 0
	global_load_dwordx4 v[58:61], v231, s[4:5] offset:0
	global_load_dwordx4 v[62:65], v231, s[4:5] offset:0x400
	global_load_dwordx4 v[66:69], v231, s[4:5] offset:0x800
	global_load_dwordx4 v[70:73], v231, s[4:5] offset:0xc00
	s_waitcnt vmcnt(8)
	s_nop 0
	v_add_u32_e32 v40, 0x10000, v36
	v_cvt_pk_bf16_f32 v36, v2, v6
	v_cvt_pk_bf16_f32 v37, v10, v14
	v_cvt_pk_bf16_f32 v38, v18, v22
	v_cvt_pk_bf16_f32 v39, v26, v30
	ds_write_b128 v40, v[36:39]
	s_nop 1
	v_cvt_pk_bf16_f32 v36, v3, v7
	v_cvt_pk_bf16_f32 v37, v11, v15
	v_cvt_pk_bf16_f32 v38, v19, v23
	v_cvt_pk_bf16_f32 v39, v27, v31
	v_xor_b32_e32 v2, 64, v40
	ds_write_b128 v2, v[36:39]
	s_nop 1
	v_cvt_pk_bf16_f32 v36, v4, v8
	v_cvt_pk_bf16_f32 v37, v12, v16
	v_cvt_pk_bf16_f32 v38, v20, v24
	v_cvt_pk_bf16_f32 v39, v28, v32
	v_xor_b32_e32 v2, 0x80, v40
	ds_write_b128 v2, v[36:39]
	s_nop 1
	v_cvt_pk_bf16_f32 v2, v5, v9
	v_cvt_pk_bf16_f32 v3, v13, v17
	v_cvt_pk_bf16_f32 v4, v21, v25
	v_cvt_pk_bf16_f32 v5, v29, v33
	v_xor_b32_e32 v6, 0xc0, v40
	ds_write_b128 v6, v[2:5]
	s_nop 1
	s_add_u32 s4, s20, 0x20000
	s_addc_u32 s5, s21, 0
	global_load_dwordx4 v[2:5], v231, s[4:5] offset:0
	global_load_dwordx4 v[6:9], v231, s[4:5] offset:0x400
	global_load_dwordx4 v[10:13], v231, s[4:5] offset:0x800
	global_load_dwordx4 v[14:17], v231, s[4:5] offset:0xc00
	s_add_u32 s4, s4, 0x1000
	s_addc_u32 s5, s5, 0
	global_load_dwordx4 v[18:21], v231, s[4:5] offset:0
	global_load_dwordx4 v[22:25], v231, s[4:5] offset:0x400
	global_load_dwordx4 v[26:29], v231, s[4:5] offset:0x800
	global_load_dwordx4 v[30:33], v231, s[4:5] offset:0xc00
	v_mov_b32_e32 v36, v232
	s_nop 0
	s_waitcnt vmcnt(8)
	s_nop 0
	v_add_u32_e32 v40, 0x18000, v36
	v_cvt_pk_bf16_f32 v36, v42, v46
	v_cvt_pk_bf16_f32 v37, v50, v54
	v_cvt_pk_bf16_f32 v38, v58, v62
	v_cvt_pk_bf16_f32 v39, v66, v70
	ds_write_b128 v40, v[36:39]
	s_nop 1
	v_cvt_pk_bf16_f32 v36, v43, v47
	v_cvt_pk_bf16_f32 v37, v51, v55
	v_cvt_pk_bf16_f32 v38, v59, v63
	v_cvt_pk_bf16_f32 v39, v67, v71
	v_xor_b32_e32 v41, 0x40, v40
	ds_write_b128 v41, v[36:39]
	s_nop 1
	v_cvt_pk_bf16_f32 v36, v44, v48
	v_cvt_pk_bf16_f32 v37, v52, v56
	v_cvt_pk_bf16_f32 v38, v60, v64
	v_cvt_pk_bf16_f32 v39, v68, v72
	v_xor_b32_e32 v41, 0x80, v40
	ds_write_b128 v41, v[36:39]
	s_nop 1
	v_cvt_pk_bf16_f32 v36, v45, v49
	v_cvt_pk_bf16_f32 v37, v53, v57
	v_cvt_pk_bf16_f32 v38, v61, v65
	v_cvt_pk_bf16_f32 v39, v69, v73
	v_xor_b32_e32 v41, 0xc0, v40
	ds_write_b128 v41, v[36:39]
	s_nop 1
	s_waitcnt vmcnt(8)
	s_waitcnt lgkmcnt(0)
	s_cmp_eq_u32 s0, 1
	s_cselect_b64 s[10:11], -1, 0
	s_cmp_lg_u32 s0, 1
	s_cbranch_scc1 .LBB0_2235
	s_barrier

; #define PG8_BWAIT(n) asm volatile("s_waitcnt vmcnt(" #n ")" : "+v"(bv[0]), "+v"(bv[1]), "+v"(bv[2]), "+v"(bv[3]), "+v"(bv[4]), "+v"(bv[5]), "+v"(bv[6]), "+v"(bv[7]) :: "memory")
; #define PG8_STAGE_A(bufoff, V0, V1, kb) do { \
;         __builtin_amdgcn_global_load_lds((const unsigned*)((Abase + (kb)) + (V0)), (LAS unsigned*)(lds + (bufoff) + ldsw), 16, 0, 0); \
;         __builtin_amdgcn_global_load_lds((const unsigned*)((Abase + (kb)) + (V1)), (LAS unsigned*)(lds + (bufoff) + ldsw + 8192), 16, 0, 0); } while (0)
; #define PG8_SCHED __builtin_amdgcn_sched_barrier(0)
;     __device__ __forceinline__ int blane(int rho) const { if constexpr (NPN == 2) return rho; else return 64 * (rho >> 5) + 16 * ((rho >> 3) & 3) + (rho & 7); }
; template <class Epi, class Sched, bool ALIGN_EPI>
; __device__ __forceinline__ void gemm_phase(LAS unsigned char* lds, const Gemm g, const Sched& S, const Epi& E) {
;     ...
;     [[maybe_unused]] const int bh = wid >> 2, brg = ((wid & 3) << 3) + (lane & 7), bkg = lane >> 3;
;     [[maybe_unused]] const int brho = 32 * (brg >> 3) + 8 * (brg & 3) + 4 * ((brg >> 2) & 1);
;     [[maybe_unused]] const int bwofs = bh * HTB + lds_byte(4 * brg, 8 * bkg);
;     [[maybe_unused]] const unsigned blane = (unsigned)(S.blane(brho) + 8 * bkg * Sched::LDN) * 4u;
;     [[maybe_unused]] const unsigned bwaddr = ((unsigned)(size_t)lds + (unsigned)bwofs) | ((unsigned)(brg & 3) << 6);
;     ...
;         PG8_BISSUE(pbc);
;         PG8_STAGE_A(PG8_SA(0, 0), vc00, vc01, 0u); PG8_STAGE_A(PG8_SA(0, 1), vc10, vc11, 0u); PG8_STAGE_A(PG8_SA(1, 0), vc00, vc01, 128u);
;         PG8_BWAIT(0); PG8_BCOMMIT(0); PG8_SCHED; PG8_BISSUE(pbc + (size_t)64 * Sched::LDN);
;         PG8_BWAIT(0); PG8_BCOMMIT(1); PG8_SCHED; PG8_BISSUE(pbc + (size_t)128 * Sched::LDN);
.LBB0_2429:
	s_ashr_i32 s6, s7, 6
	s_and_b32 s0, s6, 3
	v_and_b32_e32 v36, 3, v1
	s_lshl_b32 s12, s6, 10
	v_and_b32_e32 v2, 56, v1
	v_and_b32_e32 v3, 4, v1
	v_lshlrev_b32_e32 v4, 4, v36
	s_lshl_b32 s6, s0, 6
	v_or3_b32 v3, v4, v3, s6
	v_lshlrev_b32_e32 v2, 12, v2
	v_lshl_or_b32 v240, v3, 2, v2
	v_and_b32_e32 v3, 7, v1
	v_lshl_add_u32 v3, v3, 4, v2
	v_lshrrev_b32_e32 v4, 8, v1
	v_mul_u32_u24_e32 v4, 0x60, v4
	v_lshrrev_b32_e32 v240, 6, v1
	v_and_b32_e32 v240, 3, v240
	v_lshl_add_u32 v4, v240, 8, v4
	v_add_u32_e32 v240, v3, v4
	v_mov_b32_e32 v2, v1
	v_mov_b32_e32 v241, 1
	v_ashrrev_i32_e32 v4, 31, v2
	v_lshrrev_b32_e32 v4, 26, v4
	v_lshlrev_b32_e32 v3, 4, v2
	v_add_u32_e32 v4, v2, v4
	v_bfe_i32 v2, v2, 27, 1
	v_lshrrev_b32_e32 v2, 22, v2
	v_add_u32_e32 v2, v3, v2
	v_and_b32_e32 v2, 0xfffffc00, v2
	v_sub_u32_e32 v2, v3, v2
	v_lshrrev_b32_e32 v5, 4, v2
	v_bitop3_b32 v2, v5, v2, 32 bitop3:0x6c
	v_ashrrev_i32_e32 v6, 31, v2
	v_lshrrev_b32_e32 v6, 26, v6
	v_add_u32_e32 v6, v2, v6
	v_ashrrev_i32_e32 v7, 6, v6
	v_and_b32_e32 v6, 0xc0, v6
	v_ashrrev_i32_e32 v4, 6, v4
	v_sub_u32_e32 v2, v2, v6
	v_lshlrev_b32_e32 v5, 3, v4
	v_lshlrev_b32_e32 v4, 5, v4
	v_ashrrev_i16_sdwa v2, v241, sext(v2) dst_sel:DWORD dst_unused:UNUSED_PAD src0_sel:DWORD src1_sel:BYTE_0
	v_and_b32_e32 v4, 32, v4
	v_bfe_i32 v2, v2, 0, 16
	v_add_lshl_u32 v34, v4, v2, 1
	v_add_u32_e32 v2, 0x2000, v3
	v_ashrrev_i32_e32 v3, 31, v2
	v_lshrrev_b32_e32 v3, 22, v3
	v_add_u32_e32 v3, v2, v3
	v_ashrrev_i32_e32 v3, 10, v3
	v_mul_i32_i24_e32 v4, 0x400, v3
	v_sub_u32_e32 v2, v2, v4
	v_lshrrev_b32_e32 v4, 4, v2
	v_bitop3_b32 v2, v4, v2, 32 bitop3:0x6c
	v_ashrrev_i32_e32 v6, 31, v2
	v_lshrrev_b32_e32 v6, 26, v6
	v_and_b32_e32 v5, -16, v5
	v_add_u32_e32 v6, v2, v6
	v_add_u32_e32 v5, v7, v5
	v_ashrrev_i32_e32 v7, 6, v6
	v_and_b32_e32 v6, 0xc0, v6
	v_sub_u32_e32 v2, v2, v6
	s_ashr_i32 s1, s7, 8
	v_lshlrev_b32_e32 v4, 3, v3
	v_lshlrev_b32_e32 v3, 5, v3
	v_ashrrev_i16_sdwa v2, v241, sext(v2) dst_sel:DWORD dst_unused:UNUSED_PAD src0_sel:DWORD src1_sel:BYTE_0
	s_lshl_b32 s8, s1, 14
	v_and_b32_e32 v4, -16, v4
	v_and_b32_e32 v3, 32, v3
	v_bfe_i32 v2, v2, 0, 16
	s_add_i32 s13, s8, 0
	v_add_u32_e32 v4, v7, v4
	v_add_lshl_u32 v35, v3, v2, 1
	v_add_u32_e32 v2, s41, v5
	s_add_i32 s8, s34, -1
	v_min_i32_e32 v37, s8, v2
	v_add_u32_e32 v2, s41, v4
	s_add_i32 s9, s41, 0x80
	v_min_i32_e32 v38, s8, v2
	v_add_u32_e32 v2, s9, v5
	v_min_i32_e32 v39, s8, v2
	v_add_u32_e32 v2, s9, v4
	v_min_i32_e32 v40, s8, v2
	s_add_u32 s8, s76, s4
	s_addc_u32 s9, s77, s5
	s_lshl_b32 s4, s33, 8
	s_ashr_i32 s5, s4, 31
	s_lshl_b64 s[4:5], s[4:5], 2
	s_add_u32 s10, s8, s4
	s_addc_u32 s11, s9, s5
	s_lshl_b32 s4, s1, 3
	s_ashr_i32 s5, s4, 31
	s_lshl_b64 s[8:9], s[4:5], 2
	s_add_u32 s4, s10, s8
	s_addc_u32 s5, s11, s9
	s_add_u32 s10, s4, 0x1000
	global_load_dwordx4 v[2:5], v240, s[4:5] offset:0
	s_addc_u32 s11, s5, 0
	global_load_dwordx4 v[6:9], v240, s[10:11] offset:0
	s_add_u32 s10, s4, 0x2000
	s_addc_u32 s11, s5, 0
	global_load_dwordx4 v[10:13], v240, s[10:11] offset:0
	s_add_u32 s10, s4, 0x3000
	s_addc_u32 s11, s5, 0
	global_load_dwordx4 v[14:17], v240, s[10:11] offset:0
	s_add_u32 s10, s4, 0x4000
	s_addc_u32 s11, s5, 0
	global_load_dwordx4 v[18:21], v240, s[10:11] offset:0
	s_add_u32 s10, s4, 0x5000
	s_addc_u32 s11, s5, 0
	global_load_dwordx4 v[22:25], v240, s[10:11] offset:0
	s_add_u32 s10, s4, 0x6000
	s_addc_u32 s11, s5, 0
	global_load_dwordx4 v[26:29], v240, s[10:11] offset:0
	s_add_u32 s10, s4, 0x7000
	s_addc_u32 s11, s5, 0
	global_load_dwordx4 v[30:33], v240, s[10:11] offset:0
	s_add_i32 s35, s12, 0
	v_readlane_b32 s10, v254, 53
	v_lshl_add_u32 v226, v37, 9, v34
	s_mov_b32 m0, s35
	v_readlane_b32 s11, v254, 54
	s_add_i32 s36, s35, 0x2000
	v_lshl_add_u32 v228, v38, 9, v35
	s_add_i32 s37, s35, 0x4000
	v_lshl_add_u32 v230, v39, 9, v34
	s_add_i32 s38, s35, 0x6000
	global_load_lds_dwordx4 v226, s[10:11]
	s_mov_b32 m0, s36
	v_lshl_add_u32 v232, v40, 9, v35
	global_load_lds_dwordx4 v228, s[10:11]
	s_mov_b32 m0, s37
	v_lshlrev_b32_e32 v34, 2, v1
	global_load_lds_dwordx4 v230, s[10:11]
	s_mov_b32 m0, s38
	v_and_b32_e32 v35, 16, v34
	global_load_lds_dwordx4 v232, s[10:11]
	s_add_u32 s10, s90, 0x27340080
	s_addc_u32 s11, s91, 0
	s_add_i32 s39, s35, 0x8000
	s_mov_b32 m0, s39
	s_add_i32 s40, s35, 0xa000
	global_load_lds_dwordx4 v226, s[10:11]
	s_mov_b32 m0, s40
	v_lshl_or_b32 v35, s0, 5, v35
	global_load_lds_dwordx4 v228, s[10:11]
	v_lshrrev_b32_e32 v35, 3, v35
	v_bfe_u32 v37, v1, 5, 1
	v_or_b32_e32 v35, v35, v37
	v_lshlrev_b32_e32 v37, 8, v1
	v_lshlrev_b32_e32 v38, 1, v1
	v_lshlrev_b32_e32 v39, 10, v35
	v_lshlrev_b32_e32 v35, 4, v1
	v_and_b32_e32 v37, 0x300, v37
	v_and_b32_e32 v38, 48, v38
	v_and_b32_e32 v40, 32, v35
	v_bitop3_b32 v37, v37, v40, v38 bitop3:0x36
	v_add3_u32 v37, s13, v37, v39
	v_lshl_or_b32 v242, v36, 6, v37
	v_lshrrev_b32_e32 v39, 8, v1
	v_lshrrev_b32_e32 v36, 2, v1
	v_and_b32_e32 v36, 1, v36
	v_lshl_or_b32 v36, v39, 1, v36
	v_lshlrev_b32_e32 v37, 8, v36
	v_lshl_or_b32 v37, v36, 6, v37
	v_lshlrev_b32_e32 v38, 1, v1
	v_and_b32_e32 v38, 48, v38
	v_or_b32_e32 v37, v37, v38
	v_lshlrev_b32_e32 v38, 5, v39
	v_xor_b32_e32 v37, v37, v38
	v_lshlrev_b32_e32 v38, 13, v1
	v_and_b32_e32 v38, 0x4000, v38
	v_or_b32_e32 v37, v37, v38
	v_and_b32_e32 v38, 1, v1
	v_bfe_u32 v36, v1, 5, 1
	v_lshl_or_b32 v38, v38, 1, v36
	v_lshrrev_b32_e32 v39, 6, v1
	v_and_b32_e32 v39, 3, v39
	v_lshl_or_b32 v38, v39, 2, v38
	v_lshl_or_b32 v242, v38, 10, v37
	v_mov_b32_e32 v36, v242
	s_add_u32 s12, s4, 0x40000
	s_addc_u32 s13, s5, 0
	s_add_u32 s14, s12, 0x1000
	global_load_dwordx4 v[42:45], v240, s[12:13] offset:0
	s_addc_u32 s15, s13, 0
	global_load_dwordx4 v[46:49], v240, s[14:15] offset:0
	s_add_u32 s14, s12, 0x2000
	s_addc_u32 s15, s13, 0
	global_load_dwordx4 v[50:53], v240, s[14:15] offset:0
	s_add_u32 s14, s12, 0x3000
	s_addc_u32 s15, s13, 0
	global_load_dwordx4 v[54:57], v240, s[14:15] offset:0
	s_add_u32 s14, s12, 0x4000
	s_addc_u32 s15, s13, 0
	global_load_dwordx4 v[58:61], v240, s[14:15] offset:0
	s_add_u32 s14, s12, 0x5000
	s_addc_u32 s15, s13, 0
	global_load_dwordx4 v[62:65], v240, s[14:15] offset:0
	s_add_u32 s14, s12, 0x6000
	s_addc_u32 s15, s13, 0
	global_load_dwordx4 v[66:69], v240, s[14:15] offset:0
	s_add_u32 s12, s12, 0x7000
	s_addc_u32 s13, s13, 0
	global_load_dwordx4 v[70:73], v240, s[12:13] offset:0
	s_waitcnt vmcnt(8)
; #define PG8_BWAIT(n) asm volatile("s_waitcnt vmcnt(" #n ")" : "+v"(bv[0]), "+v"(bv[1]), "+v"(bv[2]), "+v"(bv[3]), "+v"(bv[4]), "+v"(bv[5]), "+v"(bv[6]), "+v"(bv[7]) :: "memory")
; #define PG8_WAIT_V(n) asm volatile("s_waitcnt vmcnt(" #n ")" ::: "memory")
; #define PG8_WAIT_L(n) asm volatile("s_waitcnt lgkmcnt(" #n ")" ::: "memory")
; #define PG8_BAR __builtin_amdgcn_s_barrier()
; #define PG8_SCHED __builtin_amdgcn_sched_barrier(0)
; template <class Epi, class Sched, bool ALIGN_EPI>
; __device__ __forceinline__ void gemm_phase(LAS unsigned char* lds, const Gemm g, const Sched& S, const Epi& E) {
;     ...
;         PG8_BWAIT(0); PG8_BCOMMIT(0); PG8_SCHED; PG8_BISSUE(pbc + (size_t)64 * Sched::LDN);
;         PG8_BWAIT(0); PG8_BCOMMIT(1); PG8_SCHED; PG8_BISSUE(pbc + (size_t)128 * Sched::LDN);
;         PG8_WAIT_V(8); PG8_WAIT_L(0);
;         if (wr == 1) PG8_BAR;
;         PG8_BAR; PG8_BAR;
	s_mov_b32 s11, 0
	v_add_u32_e32 v40, 0x10000, v36
	v_cvt_pk_bf16_f32 v36, v2, v6
	v_cvt_pk_bf16_f32 v37, v10, v14
	v_cvt_pk_bf16_f32 v38, v18, v22
	v_cvt_pk_bf16_f32 v39, v26, v30
	ds_write_b128 v40, v[36:39]
	s_nop 1
	v_cvt_pk_bf16_f32 v36, v3, v7
	v_cvt_pk_bf16_f32 v37, v11, v15
	v_cvt_pk_bf16_f32 v38, v19, v23
	v_cvt_pk_bf16_f32 v39, v27, v31
	v_xor_b32_e32 v2, 64, v40
	ds_write_b128 v2, v[36:39]
	s_nop 1
	v_cvt_pk_bf16_f32 v36, v4, v8
	v_cvt_pk_bf16_f32 v37, v12, v16
	v_cvt_pk_bf16_f32 v38, v20, v24
	v_cvt_pk_bf16_f32 v39, v28, v32
	v_xor_b32_e32 v2, 0x80, v40
	ds_write_b128 v2, v[36:39]
	s_nop 1
	v_cvt_pk_bf16_f32 v2, v5, v9
	v_cvt_pk_bf16_f32 v3, v13, v17
	v_cvt_pk_bf16_f32 v4, v21, v25
	v_cvt_pk_bf16_f32 v5, v29, v33
	v_xor_b32_e32 v6, 0xc0, v40
	ds_write_b128 v6, v[2:5]
	s_nop 1
	s_add_u32 s12, s4, 0x80000
	s_addc_u32 s13, s5, 0
	s_add_u32 s14, s12, 0x1000
	global_load_dwordx4 v[2:5], v240, s[12:13] offset:0
	s_addc_u32 s15, s13, 0
	global_load_dwordx4 v[6:9], v240, s[14:15] offset:0
	s_add_u32 s14, s12, 0x2000
	s_addc_u32 s15, s13, 0
	global_load_dwordx4 v[10:13], v240, s[14:15] offset:0
	s_add_u32 s14, s12, 0x3000
	s_addc_u32 s15, s13, 0
	global_load_dwordx4 v[14:17], v240, s[14:15] offset:0
	s_add_u32 s14, s12, 0x4000
	s_addc_u32 s15, s13, 0
	global_load_dwordx4 v[18:21], v240, s[14:15] offset:0
	s_add_u32 s14, s12, 0x5000
	s_addc_u32 s15, s13, 0
	global_load_dwordx4 v[22:25], v240, s[14:15] offset:0
	s_add_u32 s14, s12, 0x6000
	s_addc_u32 s15, s13, 0
	global_load_dwordx4 v[26:29], v240, s[14:15] offset:0
	s_add_u32 s12, s12, 0x7000
	s_addc_u32 s13, s13, 0
	global_load_dwordx4 v[30:33], v240, s[12:13] offset:0
	v_mov_b32_e32 v36, v242
	s_nop 0
	s_waitcnt vmcnt(8)
	s_nop 0
	v_add_u32_e32 v40, 0x18000, v36
	v_cvt_pk_bf16_f32 v36, v42, v46
	v_cvt_pk_bf16_f32 v37, v50, v54
	v_cvt_pk_bf16_f32 v38, v58, v62
	v_cvt_pk_bf16_f32 v39, v66, v70
	ds_write_b128 v40, v[36:39]
	s_nop 1
	v_cvt_pk_bf16_f32 v36, v43, v47
	v_cvt_pk_bf16_f32 v37, v51, v55
	v_cvt_pk_bf16_f32 v38, v59, v63
	v_cvt_pk_bf16_f32 v39, v67, v71
	v_xor_b32_e32 v41, 0x40, v40
	ds_write_b128 v41, v[36:39]
	s_nop 1
	v_cvt_pk_bf16_f32 v36, v44, v48
	v_cvt_pk_bf16_f32 v37, v52, v56
	v_cvt_pk_bf16_f32 v38, v60, v64
	v_cvt_pk_bf16_f32 v39, v68, v72
	v_xor_b32_e32 v41, 0x80, v40
	ds_write_b128 v41, v[36:39]
	s_nop 1
	v_cvt_pk_bf16_f32 v36, v45, v49
	v_cvt_pk_bf16_f32 v37, v53, v57
	v_cvt_pk_bf16_f32 v38, v61, v65
	v_cvt_pk_bf16_f32 v39, v69, v73
	v_xor_b32_e32 v41, 0xc0, v40
	ds_write_b128 v41, v[36:39]
	s_nop 1
	s_waitcnt vmcnt(8)
	s_waitcnt lgkmcnt(0)
	s_cmp_eq_u32 s1, 1
	s_cselect_b64 s[12:13], -1, 0
	s_cmp_lg_u32 s1, 1
	s_cbranch_scc1 .LBB0_2431
	s_barrier

.LBB0_4693:
	v_mov_b32_e32 v2, v1
	s_add_i32 s0, s36, -1
	v_ashrrev_i32_e32 v4, 31, v2
	v_lshrrev_b32_e32 v4, 26, v4
	v_lshlrev_b32_e32 v3, 4, v2
	v_add_u32_e32 v4, v2, v4
	v_bfe_i32 v2, v2, 27, 1
	v_lshrrev_b32_e32 v2, 22, v2
	v_add_u32_e32 v2, v3, v2
	v_and_b32_e32 v2, 0xfffffc00, v2
	v_sub_u32_e32 v2, v3, v2
	v_ashrrev_i32_e32 v10, 6, v4
	v_lshrrev_b32_e32 v4, 4, v2
	v_bitop3_b32 v11, v4, v2, 32 bitop3:0x6c
	v_ashrrev_i32_e32 v4, 31, v11
	v_lshrrev_b32_e32 v4, 26, v4
	v_lshlrev_b32_e32 v2, 3, v10
	v_add_u32_e32 v12, v11, v4
	v_and_b32_e32 v2, -16, v2
	v_ashrrev_i32_e32 v4, 6, v12
	v_add_u32_e32 v6, v4, v2
	v_add_u32_e32 v2, 0x2000, v3
	v_ashrrev_i32_e32 v3, 31, v2
	v_lshrrev_b32_e32 v3, 22, v3
	v_add_u32_e32 v3, v2, v3
	v_ashrrev_i32_e32 v13, 10, v3
	v_mul_i32_i24_e32 v3, 0x400, v13
	v_sub_u32_e32 v2, v2, v3
	v_lshrrev_b32_e32 v3, 4, v2
	v_bitop3_b32 v14, v3, v2, 32 bitop3:0x6c
	v_ashrrev_i32_e32 v3, 31, v14
	v_lshrrev_b32_e32 v3, 26, v3
	v_lshlrev_b32_e32 v2, 3, v13
	v_add_u32_e32 v15, v14, v3
	v_and_b32_e32 v2, -16, v2
	v_ashrrev_i32_e32 v3, 6, v15
	v_add_u32_e32 v8, v3, v2
	v_add_u32_e32 v2, s48, v6
	v_add_u32_e32 v4, s48, v8
	s_add_i32 s1, s48, 0x80
	v_min_i32_e32 v2, s0, v2
	v_min_i32_e32 v4, s0, v4
	v_add_u32_e32 v6, s1, v6
	v_add_u32_e32 v8, s1, v8
	v_ashrrev_i32_e32 v3, 31, v2
	v_ashrrev_i32_e32 v5, 31, v4
	v_min_i32_e32 v6, s0, v6
	v_min_i32_e32 v8, s0, v8
	v_lshl_add_u64 v[2:3], v[2:3], 2, s[66:67]
	v_lshl_add_u64 v[4:5], v[4:5], 2, s[66:67]
	v_ashrrev_i32_e32 v7, 31, v6
	v_ashrrev_i32_e32 v9, 31, v8
	v_lshl_add_u64 v[6:7], v[6:7], 2, s[66:67]
	v_lshl_add_u64 v[8:9], v[8:9], 2, s[66:67]
	global_load_dword v2, v[2:3], off
	s_nop 0
	global_load_dword v3, v[4:5], off
	s_nop 0
	global_load_dword v4, v[6:7], off
	global_load_dword v5, v[8:9], off
	s_ashr_i32 s19, s4, 8
	s_ashr_i32 s1, s4, 6
	s_lshl_b32 s23, s1, 5
	s_lshl_b32 s5, s19, 14
	s_lshl_b32 s22, s1, 10
	s_and_b32 s37, s23, 0x60
	s_add_i32 s18, s5, 0
	s_cmpk_lt_u32 s4, 0x100
	s_cselect_b64 s[56:57], -1, 0
	s_and_b64 s[4:5], s[56:57], exec
	v_readlane_b32 s0, v253, 21
	v_readlane_b32 s5, v253, 26
	v_readlane_b32 s12, v253, 33
	v_readlane_b32 s14, v253, 35
	v_and_b32_e32 v36, 3, v1
	v_readlane_b32 s4, v253, 25
	v_readlane_b32 s13, v253, 34
	v_readlane_b32 s15, v253, 36
	s_cselect_b32 s5, s12, s14
	v_and_b32_e32 v7, 4, v1
	v_lshlrev_b32_e32 v8, 3, v36
	s_cselect_b32 s4, s13, s15
	s_add_u32 s38, s5, 0x10000000
	v_and_b32_e32 v6, 56, v1
	v_or3_b32 v7, v8, v7, s37
	s_addc_u32 s39, s4, 0
	v_and_b32_e32 v8, 0xc0, v12
	v_mov_b32_e32 v231, 1
	v_lshlrev_b32_e32 v6, 10, v6
	v_readlane_b32 s2, v253, 23
	s_add_u32 s4, s38, s20
	v_sub_u32_e32 v8, v11, v8
	v_lshl_or_b32 v232, v7, 2, v6
	v_lshlrev_b32_e32 v6, 5, v10
	v_readlane_b32 s3, v253, 24
	s_addc_u32 s5, s39, s21
	v_ashrrev_i16_sdwa v8, v231, sext(v8) dst_sel:DWORD dst_unused:UNUSED_PAD src0_sel:DWORD src1_sel:BYTE_0
	s_lshl_b32 s2, s33, 7
	v_and_b32_e32 v6, 32, v6
	v_bfe_i32 v8, v8, 0, 16
	v_and_b32_e32 v9, 0xc0, v15
	s_ashr_i32 s3, s2, 31
	v_add_lshl_u32 v34, v6, v8, 1
	v_sub_u32_e32 v6, v14, v9
	s_lshl_b64 s[2:3], s[2:3], 2
	v_lshlrev_b32_e32 v7, 5, v13
	v_ashrrev_i16_sdwa v6, v231, sext(v6) dst_sel:DWORD dst_unused:UNUSED_PAD src0_sel:DWORD src1_sel:BYTE_0
	s_add_u32 s20, s4, s2
	v_and_b32_e32 v7, 32, v7
	v_bfe_i32 v6, v6, 0, 16
	s_addc_u32 s21, s5, s3
	v_add_lshl_u32 v35, v7, v6, 1
	s_add_u32 s2, s20, 0x1000
	s_addc_u32 s3, s21, 0
	v_readlane_b32 s1, v253, 22
	s_add_i32 s40, s22, 0
	v_readlane_b32 s0, v255, 13
	s_mov_b32 m0, s40
	v_readlane_b32 s1, v255, 14
	s_add_i32 s41, s40, 0x2000
	s_add_i32 s42, s40, 0x4000
	s_add_i32 s43, s40, 0x6000
	v_readlane_b32 s9, v253, 30
	v_readlane_b32 s10, v253, 31
	v_readlane_b32 s11, v253, 32
	s_mov_b32 s9, 0
	v_readlane_b32 s6, v253, 27
	v_readlane_b32 s7, v253, 28
	v_readlane_b32 s8, v253, 29
	s_waitcnt vmcnt(3)
	v_lshlrev_b32_e32 v37, 8, v2
	s_waitcnt vmcnt(2)
	v_lshlrev_b32_e32 v38, 8, v3
	s_waitcnt vmcnt(1)
	v_lshlrev_b32_e32 v2, 8, v4
	s_waitcnt vmcnt(0)
; #define PG8_BWAIT(n) asm volatile("s_waitcnt vmcnt(" #n ")" : "+v"(bv[0]), "+v"(bv[1]), "+v"(bv[2]), "+v"(bv[3]), "+v"(bv[4]), "+v"(bv[5]), "+v"(bv[6]), "+v"(bv[7]) :: "memory")
; #define PG8_STAGE_A(bufoff, V0, V1, kb) do { \
;         __builtin_amdgcn_global_load_lds((const unsigned*)((Abase + (kb)) + (V0)), (LAS unsigned*)(lds + (bufoff) + ldsw), 16, 0, 0); \
;         __builtin_amdgcn_global_load_lds((const unsigned*)((Abase + (kb)) + (V1)), (LAS unsigned*)(lds + (bufoff) + ldsw + 8192), 16, 0, 0); } while (0)
; #define PG8_WAIT_V(n) asm volatile("s_waitcnt vmcnt(" #n ")" ::: "memory")
; #define PG8_WAIT_L(n) asm volatile("s_waitcnt lgkmcnt(" #n ")" ::: "memory")
; #define PG8_BAR __builtin_amdgcn_s_barrier()
; #define PG8_SCHED __builtin_amdgcn_sched_barrier(0)
; template <class Epi, class Sched, bool ALIGN_EPI>
; __device__ __forceinline__ void gemm_phase(LAS unsigned char* lds, const Gemm g, const Sched& S, const Epi& E) {
;     ...
;         PG8_BISSUE(pbc);
;         PG8_STAGE_A(PG8_SA(0, 0), vc00, vc01, 0u); PG8_STAGE_A(PG8_SA(0, 1), vc10, vc11, 0u); PG8_STAGE_A(PG8_SA(1, 0), vc00, vc01, 128u);
;         PG8_BWAIT(0); PG8_BCOMMIT(0); PG8_SCHED; PG8_BISSUE(pbc + (size_t)64 * Sched::LDN);
;         PG8_BWAIT(0); PG8_BCOMMIT(1); PG8_SCHED; PG8_BISSUE(pbc + (size_t)128 * Sched::LDN);
;         PG8_WAIT_V(8); PG8_WAIT_L(0);
;         if (wr == 1) PG8_BAR;
;         PG8_BAR; PG8_BAR;
	v_lshlrev_b32_e32 v3, 8, v5
	v_and_b32_e32 v39, 0xfffff800, v2
	v_and_b32_e32 v40, 0xfffff800, v3
	global_load_dwordx4 v[2:5], v232, s[20:21] offset:0
	global_load_dwordx4 v[6:9], v232, s[20:21] offset:0x400
	global_load_dwordx4 v[10:13], v232, s[20:21] offset:0x800
	global_load_dwordx4 v[14:17], v232, s[20:21] offset:0xc00
	global_load_dwordx4 v[18:21], v232, s[2:3] offset:0
	global_load_dwordx4 v[22:25], v232, s[2:3] offset:0x400
	global_load_dwordx4 v[26:29], v232, s[2:3] offset:0x800
	v_and_b32_e32 v37, 0xfffff800, v37
	global_load_dwordx4 v[30:33], v232, s[2:3] offset:0xc00
	v_add_u32_e32 v226, v34, v37
	v_and_b32_e32 v37, 0xfffff800, v38
	v_add_u32_e32 v228, v35, v37
	global_load_lds_dwordx4 v226, s[0:1]
	s_mov_b32 m0, s41
	v_add_u32_e32 v233, v34, v39
	global_load_lds_dwordx4 v228, s[0:1]
	s_mov_b32 m0, s42
	s_add_u32 s2, s90, 0x176c0080
	v_add_u32_e32 v234, v35, v40
	global_load_lds_dwordx4 v233, s[0:1]
	s_mov_b32 m0, s43
	s_addc_u32 s3, s91, 0
	s_add_i32 s44, s40, 0x8000
	global_load_lds_dwordx4 v234, s[0:1]
	s_mov_b32 m0, s44
	s_add_i32 s45, s40, 0xa000
	global_load_lds_dwordx4 v226, s[2:3]
	s_mov_b32 m0, s45
	v_lshlrev_b32_e32 v34, 2, v1
	global_load_lds_dwordx4 v228, s[2:3]
	v_and_or_b32 v35, v34, 16, s23
	v_lshrrev_b32_e32 v35, 3, v35
	v_bfe_u32 v37, v1, 5, 1
	v_and_or_b32 v35, v35, 14, v37
	v_lshlrev_b32_e32 v37, 8, v1
	v_lshlrev_b32_e32 v38, 1, v1
	v_lshlrev_b32_e32 v39, 10, v35
	v_lshlrev_b32_e32 v35, 4, v1
	v_and_b32_e32 v37, 0x300, v37
	v_and_b32_e32 v38, 48, v38
	v_and_b32_e32 v40, 32, v35
	v_bitop3_b32 v37, v37, v40, v38 bitop3:0x36
	v_add3_u32 v37, s18, v37, v39
	v_lshl_or_b32 v235, v36, 6, v37
	v_mov_b32_e32 v36, v235
	s_add_u32 s2, s20, 0x10000
	s_addc_u32 s3, s21, 0
	global_load_dwordx4 v[42:45], v232, s[2:3] offset:0
	global_load_dwordx4 v[46:49], v232, s[2:3] offset:0x400
	global_load_dwordx4 v[50:53], v232, s[2:3] offset:0x800
	global_load_dwordx4 v[54:57], v232, s[2:3] offset:0xc00
	s_add_u32 s2, s2, 0x1000
	s_addc_u32 s3, s3, 0
	global_load_dwordx4 v[58:61], v232, s[2:3] offset:0
	global_load_dwordx4 v[62:65], v232, s[2:3] offset:0x400
	global_load_dwordx4 v[66:69], v232, s[2:3] offset:0x800
	global_load_dwordx4 v[70:73], v232, s[2:3] offset:0xc00
	s_waitcnt vmcnt(8)
	s_nop 0
	v_add_u32_e32 v40, 0x10000, v36
	v_cvt_pk_bf16_f32 v36, v2, v6
	v_cvt_pk_bf16_f32 v37, v10, v14
	v_cvt_pk_bf16_f32 v38, v18, v22
	v_cvt_pk_bf16_f32 v39, v26, v30
	ds_write_b128 v40, v[36:39]
	s_nop 1
	v_cvt_pk_bf16_f32 v36, v3, v7
	v_cvt_pk_bf16_f32 v37, v11, v15
	v_cvt_pk_bf16_f32 v38, v19, v23
	v_cvt_pk_bf16_f32 v39, v27, v31
	v_xor_b32_e32 v2, 64, v40
	ds_write_b128 v2, v[36:39]
	s_nop 1
	v_cvt_pk_bf16_f32 v36, v4, v8
	v_cvt_pk_bf16_f32 v37, v12, v16
	v_cvt_pk_bf16_f32 v38, v20, v24
	v_cvt_pk_bf16_f32 v39, v28, v32
	v_xor_b32_e32 v2, 0x80, v40
	ds_write_b128 v2, v[36:39]
	s_nop 1
	v_cvt_pk_bf16_f32 v2, v5, v9
	v_cvt_pk_bf16_f32 v3, v13, v17
	v_cvt_pk_bf16_f32 v4, v21, v25
	v_cvt_pk_bf16_f32 v5, v29, v33
	v_xor_b32_e32 v6, 0xc0, v40
	ds_write_b128 v6, v[2:5]
	s_nop 1
	s_add_u32 s2, s20, 0x20000
	s_addc_u32 s3, s21, 0
	global_load_dwordx4 v[2:5], v232, s[2:3] offset:0
	global_load_dwordx4 v[6:9], v232, s[2:3] offset:0x400
	global_load_dwordx4 v[10:13], v232, s[2:3] offset:0x800
	global_load_dwordx4 v[14:17], v232, s[2:3] offset:0xc00
	s_add_u32 s2, s2, 0x1000
	s_addc_u32 s3, s3, 0
	global_load_dwordx4 v[18:21], v232, s[2:3] offset:0
	global_load_dwordx4 v[22:25], v232, s[2:3] offset:0x400
	global_load_dwordx4 v[26:29], v232, s[2:3] offset:0x800
	global_load_dwordx4 v[30:33], v232, s[2:3] offset:0xc00
	v_mov_b32_e32 v36, v235
	s_nop 0
	s_waitcnt vmcnt(8)
	s_nop 0
	v_add_u32_e32 v40, 0x18000, v36
	v_cvt_pk_bf16_f32 v36, v42, v46
	v_cvt_pk_bf16_f32 v37, v50, v54
	v_cvt_pk_bf16_f32 v38, v58, v62
	v_cvt_pk_bf16_f32 v39, v66, v70
	ds_write_b128 v40, v[36:39]
	s_nop 1
	v_cvt_pk_bf16_f32 v36, v43, v47
	v_cvt_pk_bf16_f32 v37, v51, v55
	v_cvt_pk_bf16_f32 v38, v59, v63
	v_cvt_pk_bf16_f32 v39, v67, v71
	v_xor_b32_e32 v41, 0x40, v40
	ds_write_b128 v41, v[36:39]
	s_nop 1
	v_cvt_pk_bf16_f32 v36, v44, v48
	v_cvt_pk_bf16_f32 v37, v52, v56
	v_cvt_pk_bf16_f32 v38, v60, v64
	v_cvt_pk_bf16_f32 v39, v68, v72
	v_xor_b32_e32 v41, 0x80, v40
	ds_write_b128 v41, v[36:39]
	s_nop 1
	v_cvt_pk_bf16_f32 v36, v45, v49
	v_cvt_pk_bf16_f32 v37, v53, v57
	v_cvt_pk_bf16_f32 v38, v61, v65
	v_cvt_pk_bf16_f32 v39, v69, v73
	v_xor_b32_e32 v41, 0xc0, v40
	ds_write_b128 v41, v[36:39]
	s_nop 1
	s_waitcnt vmcnt(8)
	s_waitcnt lgkmcnt(0)
	s_cmp_eq_u32 s19, 1
	s_cselect_b64 s[10:11], -1, 0
	s_cmp_lg_u32 s19, 1
	s_cbranch_scc1 .LBB0_4695
	s_barrier

; #define PG8_BWAIT(n) asm volatile("s_waitcnt vmcnt(" #n ")" : "+v"(bv[0]), "+v"(bv[1]), "+v"(bv[2]), "+v"(bv[3]), "+v"(bv[4]), "+v"(bv[5]), "+v"(bv[6]), "+v"(bv[7]) :: "memory")
; #define PG8_STAGE_A(bufoff, V0, V1, kb) do { \
;         __builtin_amdgcn_global_load_lds((const unsigned*)((Abase + (kb)) + (V0)), (LAS unsigned*)(lds + (bufoff) + ldsw), 16, 0, 0); \
;         __builtin_amdgcn_global_load_lds((const unsigned*)((Abase + (kb)) + (V1)), (LAS unsigned*)(lds + (bufoff) + ldsw + 8192), 16, 0, 0); } while (0)
; #define PG8_SCHED __builtin_amdgcn_sched_barrier(0)
;     __device__ __forceinline__ int blane(int rho) const { if constexpr (NPN == 2) return rho; else return 64 * (rho >> 5) + 16 * ((rho >> 3) & 3) + (rho & 7); }
; template <class Epi, class Sched, bool ALIGN_EPI>
; __device__ __forceinline__ void gemm_phase(LAS unsigned char* lds, const Gemm g, const Sched& S, const Epi& E) {
;     ...
;     [[maybe_unused]] const int bh = wid >> 2, brg = ((wid & 3) << 3) + (lane & 7), bkg = lane >> 3;
;     [[maybe_unused]] const int brho = 32 * (brg >> 3) + 8 * (brg & 3) + 4 * ((brg >> 2) & 1);
;     [[maybe_unused]] const int bwofs = bh * HTB + lds_byte(4 * brg, 8 * bkg);
;     [[maybe_unused]] const unsigned blane = (unsigned)(S.blane(brho) + 8 * bkg * Sched::LDN) * 4u;
;     [[maybe_unused]] const unsigned bwaddr = ((unsigned)(size_t)lds + (unsigned)bwofs) | ((unsigned)(brg & 3) << 6);
;     ...
;         PG8_BISSUE(pbc);
;         PG8_STAGE_A(PG8_SA(0, 0), vc00, vc01, 0u); PG8_STAGE_A(PG8_SA(0, 1), vc10, vc11, 0u); PG8_STAGE_A(PG8_SA(1, 0), vc00, vc01, 128u);
;         PG8_BWAIT(0); PG8_BCOMMIT(0); PG8_SCHED; PG8_BISSUE(pbc + (size_t)64 * Sched::LDN);
;         PG8_BWAIT(0); PG8_BCOMMIT(1); PG8_SCHED; PG8_BISSUE(pbc + (size_t)128 * Sched::LDN);
.LBB0_4889:
	s_ashr_i32 s4, s5, 6
	s_and_b32 s0, s4, 3
	v_and_b32_e32 v36, 3, v1
	s_lshl_b32 s10, s4, 10
	v_and_b32_e32 v2, 56, v1
	v_and_b32_e32 v3, 4, v1
	v_lshlrev_b32_e32 v4, 4, v36
	s_lshl_b32 s4, s0, 6
	v_or3_b32 v3, v4, v3, s4
	v_lshlrev_b32_e32 v2, 12, v2
	v_lshl_or_b32 v240, v3, 2, v2
	v_and_b32_e32 v3, 7, v1
	v_lshl_add_u32 v3, v3, 4, v2
	v_lshrrev_b32_e32 v4, 8, v1
	v_mul_u32_u24_e32 v4, 0x60, v4
	v_lshrrev_b32_e32 v240, 6, v1
	v_and_b32_e32 v240, 3, v240
	v_lshl_add_u32 v4, v240, 8, v4
	v_add_u32_e32 v240, v3, v4
	v_mov_b32_e32 v2, v1
	v_mov_b32_e32 v241, 1
	v_ashrrev_i32_e32 v4, 31, v2
	v_lshrrev_b32_e32 v4, 26, v4
	v_lshlrev_b32_e32 v3, 4, v2
	v_add_u32_e32 v4, v2, v4
	v_bfe_i32 v2, v2, 27, 1
	v_lshrrev_b32_e32 v2, 22, v2
	v_add_u32_e32 v2, v3, v2
	v_and_b32_e32 v2, 0xfffffc00, v2
	v_sub_u32_e32 v2, v3, v2
	v_lshrrev_b32_e32 v5, 4, v2
	v_bitop3_b32 v2, v5, v2, 32 bitop3:0x6c
	v_ashrrev_i32_e32 v6, 31, v2
	v_lshrrev_b32_e32 v6, 26, v6
	v_add_u32_e32 v6, v2, v6
	v_ashrrev_i32_e32 v7, 6, v6
	v_and_b32_e32 v6, 0xc0, v6
	v_ashrrev_i32_e32 v4, 6, v4
	v_sub_u32_e32 v2, v2, v6
	v_lshlrev_b32_e32 v5, 3, v4
	v_lshlrev_b32_e32 v4, 5, v4
	v_ashrrev_i16_sdwa v2, v241, sext(v2) dst_sel:DWORD dst_unused:UNUSED_PAD src0_sel:DWORD src1_sel:BYTE_0
	v_and_b32_e32 v4, 32, v4
	v_bfe_i32 v2, v2, 0, 16
	v_add_lshl_u32 v34, v4, v2, 1
	v_add_u32_e32 v2, 0x2000, v3
	v_ashrrev_i32_e32 v3, 31, v2
	v_lshrrev_b32_e32 v3, 22, v3
	v_add_u32_e32 v3, v2, v3
	v_ashrrev_i32_e32 v3, 10, v3
	v_mul_i32_i24_e32 v4, 0x400, v3
	v_sub_u32_e32 v2, v2, v4
	v_lshrrev_b32_e32 v4, 4, v2
	v_bitop3_b32 v2, v4, v2, 32 bitop3:0x6c
	v_ashrrev_i32_e32 v6, 31, v2
	v_lshrrev_b32_e32 v6, 26, v6
	v_and_b32_e32 v5, -16, v5
	v_add_u32_e32 v6, v2, v6
	s_ashr_i32 s1, s5, 8
	v_add_u32_e32 v5, v7, v5
	v_ashrrev_i32_e32 v7, 6, v6
	v_and_b32_e32 v6, 0xc0, v6
	s_lshl_b32 s6, s1, 14
	v_sub_u32_e32 v2, v2, v6
	s_add_i32 s11, s6, 0
	v_lshlrev_b32_e32 v4, 3, v3
	v_lshlrev_b32_e32 v3, 5, v3
	v_ashrrev_i16_sdwa v2, v241, sext(v2) dst_sel:DWORD dst_unused:UNUSED_PAD src0_sel:DWORD src1_sel:BYTE_0
	s_add_u32 s34, s76, 0x10000000
	v_and_b32_e32 v4, -16, v4
	v_and_b32_e32 v3, 32, v3
	v_bfe_i32 v2, v2, 0, 16
	s_addc_u32 s35, s77, 0
	v_add_u32_e32 v4, v7, v4
	v_add_lshl_u32 v35, v3, v2, 1
	v_add_u32_e32 v2, s43, v5
	s_add_i32 s6, s36, -1
	v_min_i32_e32 v37, s6, v2
	v_add_u32_e32 v2, s43, v4
	s_add_i32 s7, s43, 0x80
	v_min_i32_e32 v38, s6, v2
	v_add_u32_e32 v2, s7, v5
	v_min_i32_e32 v39, s6, v2
	v_add_u32_e32 v2, s7, v4
	v_min_i32_e32 v40, s6, v2
	s_add_u32 s6, s34, s2
	s_addc_u32 s7, s35, s3
	s_lshl_b32 s2, s33, 8
	s_ashr_i32 s3, s2, 31
	s_lshl_b64 s[2:3], s[2:3], 2
	s_add_u32 s8, s6, s2
	s_addc_u32 s9, s7, s3
	s_lshl_b32 s2, s1, 3
	s_ashr_i32 s3, s2, 31
	s_lshl_b64 s[6:7], s[2:3], 2
	s_add_u32 s2, s8, s6
	s_addc_u32 s3, s9, s7
	s_add_u32 s8, s2, 0x1000
	global_load_dwordx4 v[2:5], v240, s[2:3] offset:0
	s_addc_u32 s9, s3, 0
	global_load_dwordx4 v[6:9], v240, s[8:9] offset:0
	s_add_u32 s8, s2, 0x2000
	s_addc_u32 s9, s3, 0
	global_load_dwordx4 v[10:13], v240, s[8:9] offset:0
	s_add_u32 s8, s2, 0x3000
	s_addc_u32 s9, s3, 0
	global_load_dwordx4 v[14:17], v240, s[8:9] offset:0
	s_add_u32 s8, s2, 0x4000
	s_addc_u32 s9, s3, 0
	global_load_dwordx4 v[18:21], v240, s[8:9] offset:0
	s_add_u32 s8, s2, 0x5000
	s_addc_u32 s9, s3, 0
	global_load_dwordx4 v[22:25], v240, s[8:9] offset:0
	s_add_u32 s8, s2, 0x6000
	s_addc_u32 s9, s3, 0
	global_load_dwordx4 v[26:29], v240, s[8:9] offset:0
	s_add_u32 s8, s2, 0x7000
	s_addc_u32 s9, s3, 0
	global_load_dwordx4 v[30:33], v240, s[8:9] offset:0
	s_add_i32 s37, s10, 0
	v_readlane_b32 s8, v254, 53
	v_lshl_add_u32 v226, v37, 9, v34
	s_mov_b32 m0, s37
	v_readlane_b32 s9, v254, 54
	s_add_i32 s38, s37, 0x2000
	v_lshl_add_u32 v228, v38, 9, v35
	s_add_i32 s39, s37, 0x4000
	v_lshl_add_u32 v230, v39, 9, v34
	s_add_i32 s40, s37, 0x6000
	global_load_lds_dwordx4 v226, s[8:9]
	s_mov_b32 m0, s38
	v_lshl_add_u32 v232, v40, 9, v35
	global_load_lds_dwordx4 v228, s[8:9]
	s_mov_b32 m0, s39
	v_lshlrev_b32_e32 v34, 2, v1
	global_load_lds_dwordx4 v230, s[8:9]
	s_mov_b32 m0, s40
	v_and_b32_e32 v35, 16, v34
	global_load_lds_dwordx4 v232, s[8:9]
	s_add_u32 s8, s90, 0x27340080
	s_addc_u32 s9, s91, 0
	s_add_i32 s41, s37, 0x8000
	s_mov_b32 m0, s41
	s_add_i32 s42, s37, 0xa000
	global_load_lds_dwordx4 v226, s[8:9]
	s_mov_b32 m0, s42
	v_lshl_or_b32 v35, s0, 5, v35
	global_load_lds_dwordx4 v228, s[8:9]
	v_lshrrev_b32_e32 v35, 3, v35
	v_bfe_u32 v37, v1, 5, 1
	v_or_b32_e32 v35, v35, v37
	v_lshlrev_b32_e32 v37, 8, v1
	v_lshlrev_b32_e32 v38, 1, v1
	v_lshlrev_b32_e32 v39, 10, v35
	v_lshlrev_b32_e32 v35, 4, v1
	v_and_b32_e32 v37, 0x300, v37
	v_and_b32_e32 v38, 48, v38
	v_and_b32_e32 v40, 32, v35
	v_bitop3_b32 v37, v37, v40, v38 bitop3:0x36
	v_add3_u32 v37, s11, v37, v39
	v_lshl_or_b32 v242, v36, 6, v37
	v_lshrrev_b32_e32 v39, 8, v1
	v_lshrrev_b32_e32 v36, 2, v1
	v_and_b32_e32 v36, 1, v36
	v_lshl_or_b32 v36, v39, 1, v36
	v_lshlrev_b32_e32 v37, 8, v36
	v_lshl_or_b32 v37, v36, 6, v37
	v_lshlrev_b32_e32 v38, 1, v1
	v_and_b32_e32 v38, 48, v38
	v_or_b32_e32 v37, v37, v38
	v_lshlrev_b32_e32 v38, 5, v39
	v_xor_b32_e32 v37, v37, v38
	v_lshlrev_b32_e32 v38, 13, v1
	v_and_b32_e32 v38, 0x4000, v38
	v_or_b32_e32 v37, v37, v38
	v_and_b32_e32 v38, 1, v1
	v_bfe_u32 v36, v1, 5, 1
	v_lshl_or_b32 v38, v38, 1, v36
	v_lshrrev_b32_e32 v39, 6, v1
	v_and_b32_e32 v39, 3, v39
	v_lshl_or_b32 v38, v39, 2, v38
	v_lshl_or_b32 v242, v38, 10, v37
	v_mov_b32_e32 v36, v242
	s_add_u32 s10, s2, 0x40000
	s_addc_u32 s11, s3, 0
	s_add_u32 s12, s10, 0x1000
	global_load_dwordx4 v[42:45], v240, s[10:11] offset:0
	s_addc_u32 s13, s11, 0
	global_load_dwordx4 v[46:49], v240, s[12:13] offset:0
	s_add_u32 s12, s10, 0x2000
	s_addc_u32 s13, s11, 0
	global_load_dwordx4 v[50:53], v240, s[12:13] offset:0
	s_add_u32 s12, s10, 0x3000
	s_addc_u32 s13, s11, 0
	global_load_dwordx4 v[54:57], v240, s[12:13] offset:0
	s_add_u32 s12, s10, 0x4000
	s_addc_u32 s13, s11, 0
	global_load_dwordx4 v[58:61], v240, s[12:13] offset:0
	s_add_u32 s12, s10, 0x5000
	s_addc_u32 s13, s11, 0
	global_load_dwordx4 v[62:65], v240, s[12:13] offset:0
	s_add_u32 s12, s10, 0x6000
	s_addc_u32 s13, s11, 0
	global_load_dwordx4 v[66:69], v240, s[12:13] offset:0
	s_add_u32 s10, s10, 0x7000
	s_addc_u32 s11, s11, 0
	global_load_dwordx4 v[70:73], v240, s[10:11] offset:0
	s_waitcnt vmcnt(8)
; #define PG8_BWAIT(n) asm volatile("s_waitcnt vmcnt(" #n ")" : "+v"(bv[0]), "+v"(bv[1]), "+v"(bv[2]), "+v"(bv[3]), "+v"(bv[4]), "+v"(bv[5]), "+v"(bv[6]), "+v"(bv[7]) :: "memory")
; #define PG8_WAIT_V(n) asm volatile("s_waitcnt vmcnt(" #n ")" ::: "memory")
; #define PG8_WAIT_L(n) asm volatile("s_waitcnt lgkmcnt(" #n ")" ::: "memory")
; #define PG8_BAR __builtin_amdgcn_s_barrier()
; #define PG8_SCHED __builtin_amdgcn_sched_barrier(0)
; template <class Epi, class Sched, bool ALIGN_EPI>
; __device__ __forceinline__ void gemm_phase(LAS unsigned char* lds, const Gemm g, const Sched& S, const Epi& E) {
;     ...
;         PG8_BWAIT(0); PG8_BCOMMIT(0); PG8_SCHED; PG8_BISSUE(pbc + (size_t)64 * Sched::LDN);
;         PG8_BWAIT(0); PG8_BCOMMIT(1); PG8_SCHED; PG8_BISSUE(pbc + (size_t)128 * Sched::LDN);
;         PG8_WAIT_V(8); PG8_WAIT_L(0);
;         if (wr == 1) PG8_BAR;
;         PG8_BAR; PG8_BAR;
	s_mov_b32 s9, 0
	v_add_u32_e32 v40, 0x10000, v36
	v_cvt_pk_bf16_f32 v36, v2, v6
	v_cvt_pk_bf16_f32 v37, v10, v14
	v_cvt_pk_bf16_f32 v38, v18, v22
	v_cvt_pk_bf16_f32 v39, v26, v30
	ds_write_b128 v40, v[36:39]
	s_nop 1
	v_cvt_pk_bf16_f32 v36, v3, v7
	v_cvt_pk_bf16_f32 v37, v11, v15
	v_cvt_pk_bf16_f32 v38, v19, v23
	v_cvt_pk_bf16_f32 v39, v27, v31
	v_xor_b32_e32 v2, 64, v40
	ds_write_b128 v2, v[36:39]
	s_nop 1
	v_cvt_pk_bf16_f32 v36, v4, v8
	v_cvt_pk_bf16_f32 v37, v12, v16
	v_cvt_pk_bf16_f32 v38, v20, v24
	v_cvt_pk_bf16_f32 v39, v28, v32
	v_xor_b32_e32 v2, 0x80, v40
	ds_write_b128 v2, v[36:39]
	s_nop 1
	v_cvt_pk_bf16_f32 v2, v5, v9
	v_cvt_pk_bf16_f32 v3, v13, v17
	v_cvt_pk_bf16_f32 v4, v21, v25
	v_cvt_pk_bf16_f32 v5, v29, v33
	v_xor_b32_e32 v6, 0xc0, v40
	ds_write_b128 v6, v[2:5]
	s_nop 1
	s_add_u32 s10, s2, 0x80000
	s_addc_u32 s11, s3, 0
	s_add_u32 s12, s10, 0x1000
	global_load_dwordx4 v[2:5], v240, s[10:11] offset:0
	s_addc_u32 s13, s11, 0
	global_load_dwordx4 v[6:9], v240, s[12:13] offset:0
	s_add_u32 s12, s10, 0x2000
	s_addc_u32 s13, s11, 0
	global_load_dwordx4 v[10:13], v240, s[12:13] offset:0
	s_add_u32 s12, s10, 0x3000
	s_addc_u32 s13, s11, 0
	global_load_dwordx4 v[14:17], v240, s[12:13] offset:0
	s_add_u32 s12, s10, 0x4000
	s_addc_u32 s13, s11, 0
	global_load_dwordx4 v[18:21], v240, s[12:13] offset:0
	s_add_u32 s12, s10, 0x5000
	s_addc_u32 s13, s11, 0
	global_load_dwordx4 v[22:25], v240, s[12:13] offset:0
	s_add_u32 s12, s10, 0x6000
	s_addc_u32 s13, s11, 0
	global_load_dwordx4 v[26:29], v240, s[12:13] offset:0
	s_add_u32 s10, s10, 0x7000
	s_addc_u32 s11, s11, 0
	global_load_dwordx4 v[30:33], v240, s[10:11] offset:0
	v_mov_b32_e32 v36, v242
	s_nop 0
	s_waitcnt vmcnt(8)
	s_nop 0
	v_add_u32_e32 v40, 0x18000, v36
	v_cvt_pk_bf16_f32 v36, v42, v46
	v_cvt_pk_bf16_f32 v37, v50, v54
	v_cvt_pk_bf16_f32 v38, v58, v62
	v_cvt_pk_bf16_f32 v39, v66, v70
	ds_write_b128 v40, v[36:39]
	s_nop 1
	v_cvt_pk_bf16_f32 v36, v43, v47
	v_cvt_pk_bf16_f32 v37, v51, v55
	v_cvt_pk_bf16_f32 v38, v59, v63
	v_cvt_pk_bf16_f32 v39, v67, v71
	v_xor_b32_e32 v41, 0x40, v40
	ds_write_b128 v41, v[36:39]
	s_nop 1
	v_cvt_pk_bf16_f32 v36, v44, v48
	v_cvt_pk_bf16_f32 v37, v52, v56
	v_cvt_pk_bf16_f32 v38, v60, v64
	v_cvt_pk_bf16_f32 v39, v68, v72
	v_xor_b32_e32 v41, 0x80, v40
	ds_write_b128 v41, v[36:39]
	s_nop 1
	v_cvt_pk_bf16_f32 v36, v45, v49
	v_cvt_pk_bf16_f32 v37, v53, v57
	v_cvt_pk_bf16_f32 v38, v61, v65
	v_cvt_pk_bf16_f32 v39, v69, v73
	v_xor_b32_e32 v41, 0xc0, v40
	ds_write_b128 v41, v[36:39]
	s_nop 1
	s_waitcnt vmcnt(8)
	s_waitcnt lgkmcnt(0)
	s_cmp_eq_u32 s1, 1
	s_cselect_b64 s[10:11], -1, 0
	s_cmp_lg_u32 s1, 1
	s_cbranch_scc1 .LBB0_4891
	s_barrier
